# expert-lists phase and its grid barrier removed: router tail scatters per-expert row/gate lists using the returned CNT atomic; gemm_gu/gemm_down index through the lists
# speedup vs baseline: 1.0544x; 1.0052x over previous
.LBB0_1420:
	s_waitcnt lgkmcnt(0)
	s_barrier
	v_cmp_gt_u32_e32 vcc, 32, v14
	s_and_saveexec_b64 s[0:1], vcc
	s_cbranch_execz .Lmy_rt_a
	v_add_u32_e32 v4, 0x20840, v1
	ds_read_b32 v5, v4
	v_readlane_b32 s2, v255, 37
	s_mov_b32 s3, 0
	s_lshl_b32 s2, s2, 6
	s_lshl_b64 s[2:3], s[2:3], 2
	s_add_u32 s2, s16, s2
	s_addc_u32 s3, s17, s3
	v_ashrrev_i32_e32 v15, 31, v14
	v_lshl_add_u64 v[2:3], v[14:15], 2, s[2:3]
	v_add_co_u32_e32 v2, vcc, 0x10000, v2
	s_nop 1
	v_addc_co_u32_e32 v3, vcc, 0, v3, vcc
	v_add_u32_e32 v7, 0x20c40, v1
	ds_write_b32 v7, v35
	s_waitcnt lgkmcnt(0)
	global_atomic_add v6, v[2:3], v5, off sc0
	v_add_u32_e32 v7, 0x20b40, v1
	s_waitcnt vmcnt(0)
	ds_write_b32 v7, v6
.Lmy_rt_a:
	s_or_b64 exec, exec, s[0:1]
	s_waitcnt vmcnt(0) lgkmcnt(0)
	s_barrier
	v_lshrrev_b32_e32 v2, 6, v14
	v_mul_lo_u32 v2, v2, s95
	v_add_u32_e32 v2, s97, v2
	s_lshr_b32 s2, s30, 4
	v_cmp_gt_u32_e32 vcc, s2, v2
	s_and_saveexec_b64 s[0:1], vcc
	s_cbranch_execz .Lmy_rt_b
	v_and_b32_e32 v3, 63, v14
	v_lshl_or_b32 v2, v2, 6, v3
	v_lshlrev_b32_e32 v3, 2, v2
	s_add_u32 s2, s16, 0x2bb88000
	s_addc_u32 s3, s17, 0
	s_add_u32 s4, s16, 0x2bbcc000
	s_addc_u32 s5, s17, 0
	s_add_u32 s6, s16, 0x2bc10000
	s_addc_u32 s7, s17, 0
	s_add_u32 s8, s16, 0xd5f8000
	s_addc_u32 s9, s17, 0
	s_add_u32 s10, s16, 0xd818000
	s_addc_u32 s11, s17, 0
	global_load_dword v4, v3, s[2:3] sc1
	global_load_dword v5, v3, s[4:5] sc1
	v_lshrrev_b32_e32 v10, 2, v2
	s_waitcnt vmcnt(0)
	v_lshlrev_b32_e32 v6, 2, v4
	v_add_u32_e32 v7, 0x20b40, v6
	v_add_u32_e32 v8, 0x20c40, v6
	ds_read_b32 v7, v7
	ds_add_rtn_u32 v8, v8, v250
	v_mul_u32_u24_e32 v9, 0x4400, v4
	s_waitcnt lgkmcnt(0)
	v_add_u32_e32 v7, v7, v8
	global_store_dword v3, v7, s[6:7]
	v_add_lshl_u32 v9, v9, v7, 2
	global_store_dword v9, v10, s[8:9]
	global_store_dword v9, v5, s[10:11]

.LBB0_1472:
	s_or_b64 exec, exec, s[2:3]
	s_waitcnt lgkmcnt(0)
	s_barrier
.LBB0_1473:
	v_readlane_b32 s0, v255, 39
	s_add_i32 s28, s0, 11
.LBB0_1559:
	s_cmp_le_i32 s86, s28
	s_cselect_b64 s[0:1], -1, 0
	s_cmp_lt_i32 s28, s87
	s_cselect_b64 s[2:3], -1, 0
	s_and_b64 s[2:3], s[0:1], s[2:3]
	s_mov_b64 s[0:1], -1
	s_and_b64 vcc, exec, s[2:3]
	s_cbranch_vccnz .LBB0_1561
	v_readlane_b32 s0, v255, 39
	s_add_i32 s28, s0, 12
	s_mov_b64 s[0:1], 0

.LBB0_1576:
	v_mov_b32_e32 v4, s66
	ds_read2_b32 v[4:5], v4 offset1:1
	s_waitcnt lgkmcnt(0)
	v_ashrrev_i32_e32 v4, 8, v4
	v_cmp_le_i32_e32 vcc, v4, v3
	v_ashrrev_i32_e32 v5, 8, v5
	s_nop 0
	v_cndmask_b32_e64 v4, 0, 1, vcc
	v_cmp_gt_i32_e32 vcc, v5, v3
	s_nop 1
	v_cndmask_b32_e32 v6, 2, v4, vcc
	v_mov_b32_e32 v4, s67
	ds_read2_b32 v[4:5], v4 offset1:1
	s_waitcnt lgkmcnt(0)
	v_ashrrev_i32_e32 v4, 8, v4
	v_cmp_gt_i32_e32 vcc, v4, v3
	v_ashrrev_i32_e32 v5, 8, v5
	s_nop 0
	v_cndmask_b32_e32 v4, 3, v6, vcc
	v_cmp_gt_i32_e32 vcc, v5, v3
	s_nop 1
	v_cndmask_b32_e32 v6, 4, v4, vcc
	v_mov_b32_e32 v4, s72
	ds_read2_b32 v[4:5], v4 offset1:1
	s_waitcnt lgkmcnt(0)
	v_ashrrev_i32_e32 v4, 8, v4
	v_cmp_gt_i32_e32 vcc, v4, v3
	v_ashrrev_i32_e32 v5, 8, v5
	s_nop 0
	v_cndmask_b32_e32 v4, 5, v6, vcc
	v_cmp_gt_i32_e32 vcc, v5, v3
	s_nop 1
	v_cndmask_b32_e32 v6, 6, v4, vcc
	v_mov_b32_e32 v4, s74
	ds_read2_b32 v[4:5], v4 offset1:1
	s_waitcnt lgkmcnt(0)
	v_ashrrev_i32_e32 v4, 8, v4
	v_cmp_gt_i32_e32 vcc, v4, v3
	v_ashrrev_i32_e32 v5, 8, v5
	s_nop 0
	v_cndmask_b32_e32 v4, 7, v6, vcc
	v_cmp_gt_i32_e32 vcc, v5, v3
	s_nop 1
	v_cndmask_b32_e32 v6, 8, v4, vcc
	v_mov_b32_e32 v4, s75
	ds_read2_b32 v[4:5], v4 offset1:1
	s_waitcnt lgkmcnt(0)
	v_ashrrev_i32_e32 v4, 8, v4
	v_cmp_gt_i32_e32 vcc, v4, v3
	v_ashrrev_i32_e32 v5, 8, v5
	s_nop 0
	v_cndmask_b32_e32 v4, 9, v6, vcc
	v_cmp_gt_i32_e32 vcc, v5, v3
	s_nop 1
	v_cndmask_b32_e32 v6, 10, v4, vcc
	v_mov_b32_e32 v4, s77
	ds_read2_b32 v[4:5], v4 offset1:1
	s_waitcnt lgkmcnt(0)
	v_ashrrev_i32_e32 v4, 8, v4
	v_cmp_gt_i32_e32 vcc, v4, v3
	v_ashrrev_i32_e32 v5, 8, v5
	s_nop 0
	v_cndmask_b32_e32 v4, 11, v6, vcc
	v_cmp_gt_i32_e32 vcc, v5, v3
	s_nop 1
	v_cndmask_b32_e32 v6, 12, v4, vcc
	v_mov_b32_e32 v4, s78
	ds_read2_b32 v[4:5], v4 offset1:1
	s_waitcnt lgkmcnt(0)
	v_ashrrev_i32_e32 v4, 8, v4
	v_cmp_gt_i32_e32 vcc, v4, v3
	v_ashrrev_i32_e32 v5, 8, v5
	s_nop 0
	v_cndmask_b32_e32 v4, 13, v6, vcc
	v_cmp_gt_i32_e32 vcc, v5, v3
	s_nop 1
	v_cndmask_b32_e32 v6, 14, v4, vcc
	v_mov_b32_e32 v4, s79
	ds_read2_b32 v[4:5], v4 offset1:1
	s_waitcnt lgkmcnt(0)
	v_ashrrev_i32_e32 v4, 8, v4
	v_cmp_gt_i32_e32 vcc, v4, v3
	v_ashrrev_i32_e32 v5, 8, v5
	s_nop 0
	v_cndmask_b32_e32 v4, 15, v6, vcc
	v_cmp_gt_i32_e32 vcc, v5, v3
	s_nop 1
	v_cndmask_b32_e32 v6, 16, v4, vcc
	v_mov_b32_e32 v4, s82
	ds_read2_b32 v[4:5], v4 offset1:1
	s_waitcnt lgkmcnt(0)
	v_ashrrev_i32_e32 v4, 8, v4
	v_cmp_gt_i32_e32 vcc, v4, v3
	v_ashrrev_i32_e32 v5, 8, v5
	s_nop 0
	v_cndmask_b32_e32 v4, 17, v6, vcc
	v_cmp_gt_i32_e32 vcc, v5, v3
	s_nop 1
	v_cndmask_b32_e32 v6, 18, v4, vcc
	v_mov_b32_e32 v4, s83
	ds_read2_b32 v[4:5], v4 offset1:1
	s_waitcnt lgkmcnt(0)
	v_ashrrev_i32_e32 v4, 8, v4
	v_cmp_gt_i32_e32 vcc, v4, v3
	v_ashrrev_i32_e32 v5, 8, v5
	s_nop 0
	v_cndmask_b32_e32 v4, 19, v6, vcc
	v_cmp_gt_i32_e32 vcc, v5, v3
	s_nop 1
	v_cndmask_b32_e32 v6, 20, v4, vcc
	v_mov_b32_e32 v4, s84
	ds_read2_b32 v[4:5], v4 offset1:1
	s_waitcnt lgkmcnt(0)
	v_ashrrev_i32_e32 v4, 8, v4
	v_cmp_gt_i32_e32 vcc, v4, v3
	v_ashrrev_i32_e32 v5, 8, v5
	s_nop 0
	v_cndmask_b32_e32 v4, 21, v6, vcc
	v_cmp_gt_i32_e32 vcc, v5, v3
	s_nop 1
	v_cndmask_b32_e32 v6, 22, v4, vcc
	v_mov_b32_e32 v4, s85
	ds_read2_b32 v[4:5], v4 offset1:1
	s_waitcnt lgkmcnt(0)
	v_ashrrev_i32_e32 v4, 8, v4
	v_cmp_gt_i32_e32 vcc, v4, v3
	v_ashrrev_i32_e32 v5, 8, v5
	s_nop 0
	v_cndmask_b32_e32 v4, 23, v6, vcc
	v_cmp_gt_i32_e32 vcc, v5, v3
	s_nop 1
	v_cndmask_b32_e32 v6, 24, v4, vcc
	v_mov_b32_e32 v4, s10
	ds_read2_b32 v[4:5], v4 offset1:1
	s_waitcnt lgkmcnt(0)
	v_ashrrev_i32_e32 v4, 8, v4
	v_cmp_gt_i32_e32 vcc, v4, v3
	v_ashrrev_i32_e32 v5, 8, v5
	s_nop 0
	v_cndmask_b32_e32 v4, 25, v6, vcc
	v_cmp_gt_i32_e32 vcc, v5, v3
	s_nop 1
	v_cndmask_b32_e32 v6, 26, v4, vcc
	v_mov_b32_e32 v4, s11
	ds_read2_b32 v[4:5], v4 offset1:1
	s_waitcnt lgkmcnt(0)
	v_ashrrev_i32_e32 v4, 8, v4
	v_cmp_gt_i32_e32 vcc, v4, v3
	v_ashrrev_i32_e32 v5, 8, v5
	s_nop 0
	v_cndmask_b32_e32 v4, 27, v6, vcc
	v_cmp_gt_i32_e32 vcc, v5, v3
	s_nop 1
	v_cndmask_b32_e32 v6, 28, v4, vcc
	v_mov_b32_e32 v4, s14
	ds_read2_b32 v[4:5], v4 offset1:1
	s_waitcnt lgkmcnt(0)
	v_ashrrev_i32_e32 v4, 8, v4
	v_cmp_gt_i32_e32 vcc, v4, v3
	v_ashrrev_i32_e32 v5, 8, v5
	s_nop 0
	v_cndmask_b32_e32 v4, 29, v6, vcc
	v_cmp_gt_i32_e32 vcc, v5, v3
	v_mov_b32_e32 v5, s65
	ds_read_b32 v5, v5
	v_cndmask_b32_e32 v4, 30, v4, vcc
	s_waitcnt lgkmcnt(0)
	v_ashrrev_i32_e32 v5, 8, v5
	v_cmp_gt_i32_e32 vcc, v5, v3
	v_add_u32_e32 v3, 0x200, v3
	s_nop 0
	v_cndmask_b32_e32 v4, 31, v4, vcc
	v_lshlrev_b32_e32 v5, 2, v4
	v_add_u32_e32 v5, 0x20840, v5
	ds_read_b32 v5, v5
	v_mul_u32_u24_e32 v6, 0x44, v4
	s_waitcnt lgkmcnt(0)
	v_ashrrev_i32_e32 v5, 8, v5
	v_sub_u32_e32 v6, v6, v5
	v_lshl_or_b32 v4, v6, 8, v4
	v_cmp_le_i32_e32 vcc, s18, v3
	ds_write_b32 v1, v4
	v_add_u32_e32 v1, 0x800, v1
	s_or_b64 s[4:5], vcc, s[4:5]
	s_andn2_b64 exec, exec, s[4:5]
	s_cbranch_execnz .LBB0_1576
.LBB0_1577:
	s_or_b64 exec, exec, s[2:3]
	v_cmp_gt_u32_e32 vcc, 0x110, v2
	s_and_saveexec_b64 s[2:3], vcc
	s_cbranch_execz .Lmy_pf_a
	s_mul_i32 s0, s97, 0x110
	v_add_u32_e32 v3, s0, v2
	s_lshl_b32 s0, s30, 2
	v_cmp_gt_u32_e32 vcc, s0, v3
	s_and_b64 exec, exec, vcc
	s_cbranch_execz .Lmy_pf_a
	v_lshlrev_b32_e32 v3, 2, v3
	s_add_u32 s4, s16, 0x2bb88000
	s_addc_u32 s5, s17, 0
	s_add_u32 s6, s16, 0x2bc10000
	s_addc_u32 s7, s17, 0
	global_load_dword v4, v3, s[4:5]
	global_load_dword v5, v3, s[6:7]
	s_waitcnt vmcnt(1)
	v_lshlrev_b32_e32 v4, 2, v4
	v_add_u32_e32 v4, 0x20840, v4
	ds_read_b32 v4, v4
	s_waitcnt vmcnt(0) lgkmcnt(0)
	v_add_u32_e32 v5, v5, v4
	global_store_dword v3, v5, s[6:7]
.Lmy_pf_a:
	s_or_b64 exec, exec, s[2:3]
	s_lshl_b32 s4, s18, 3
	s_cmp_ge_i32 s97, s4
	v_readfirstlane_b32 s19, v2
	s_waitcnt lgkmcnt(0)
	s_barrier
	s_cbranch_scc1 .LBB0_1591
	v_ashrrev_i32_e32 v1, 31, v2
	v_lshrrev_b32_e32 v1, 26, v1
	v_add_u32_e32 v1, v2, v1
	v_ashrrev_i32_e32 v4, 6, v1
	v_bfe_i32 v1, v2, 27, 1
	v_lshlrev_b32_e32 v3, 4, v2
	v_lshrrev_b32_e32 v1, 22, v1
	v_add_u32_e32 v1, v3, v1
	v_and_b32_e32 v1, 0xfffffc00, v1
	v_sub_u32_e32 v1, v3, v1
	v_lshrrev_b32_e32 v5, 4, v1
	v_bitop3_b32 v5, v5, v1, 32 bitop3:0x6c
	v_ashrrev_i32_e32 v6, 31, v5
	v_lshrrev_b32_e32 v6, 26, v6
	v_add_u32_e32 v6, v5, v6
	v_ashrrev_i32_e32 v7, 6, v6
	v_and_b32_e32 v6, 0xc0, v6
	v_sub_u32_e32 v5, v5, v6
	v_lshlrev_b32_e32 v1, 3, v4
	v_lshlrev_b32_e32 v4, 5, v4
	v_ashrrev_i16_sdwa v5, v250, sext(v5) dst_sel:DWORD dst_unused:UNUSED_PAD src0_sel:DWORD src1_sel:BYTE_0
	v_and_b32_e32 v4, 32, v4
	v_bfe_i32 v5, v5, 0, 16
	v_add_u32_e32 v3, 0x2000, v3
	v_readlane_b32 s0, v255, 37
	v_add_lshl_u32 v219, v4, v5, 1
	v_ashrrev_i32_e32 v4, 31, v3
	s_add_u32 s6, s16, 0x4578000
	v_readlane_b32 s1, v255, 38
	v_lshrrev_b32_e32 v4, 22, v4
	s_addc_u32 s7, s17, 0
	s_lshl_b64 s[0:1], s[0:1], 26
	v_add_u32_e32 v4, v3, v4
	s_add_u32 s0, s16, s0
	v_and_b32_e32 v1, -16, v1
	v_ashrrev_i32_e32 v4, 10, v4
	s_addc_u32 s1, s17, s1
	v_add_u32_e32 v1, v7, v1
	v_mul_i32_i24_e32 v5, 0x400, v4
	s_add_u32 s22, s0, 0x40eec000
	v_lshlrev_b32_e32 v6, 1, v1
	v_lshrrev_b32_e32 v8, 2, v1
	v_and_b32_e32 v7, 3, v7
	s_mov_b32 s0, 0x3fffe0
	v_sub_u32_e32 v3, v3, v5
	v_and_b32_e32 v6, 24, v6
	v_and_b32_e32 v8, 4, v8
	v_and_or_b32 v7, v1, s0, v7
	v_lshrrev_b32_e32 v5, 4, v3
	v_or3_b32 v6, v7, v8, v6
	v_bitop3_b32 v3, v5, v3, 32 bitop3:0x6c
	v_lshl_add_u32 v170, v6, 10, v219
	v_ashrrev_i32_e32 v6, 31, v3
	v_lshrrev_b32_e32 v6, 26, v6
	v_lshlrev_b32_e32 v5, 3, v4
	v_add_u32_e32 v6, v3, v6
	s_addc_u32 s23, s1, 0
	v_and_b32_e32 v5, -16, v5
	v_ashrrev_i32_e32 v7, 6, v6
	s_add_u32 s28, s16, 0xd5f8000
	v_add_u32_e32 v236, v7, v5
	v_and_b32_e32 v7, 3, v7
	s_addc_u32 s29, s17, 0
	v_and_or_b32 v7, v236, s0, v7
	s_ashr_i32 s0, s19, 6
	v_readlane_b32 s2, v254, 11
	s_add_i32 s24, s18, 1
	s_ashr_i32 s1, s19, 8
	s_lshl_b32 s25, s0, 10
	v_readlane_b32 s3, v254, 12
	s_and_b64 s[2:3], s[2:3], exec
	s_cselect_b32 s2, s24, s18
	v_readlane_b32 s3, v254, 16
	s_mul_i32 s2, s2, s3
	v_readlane_b32 s3, v254, 17
	s_add_i32 s2, s2, s3
	s_ashr_i32 s3, s2, 31
	s_lshr_b32 s3, s3, 26
	s_add_i32 s3, s2, s3
	s_ashr_i32 s5, s3, 6
	v_and_b32_e32 v5, 0xc0, v6
	s_lshl_b32 s5, s5, 3
	v_sub_u32_e32 v3, v3, v5
	s_sub_i32 s8, s18, s5
	v_lshlrev_b32_e32 v4, 5, v4
	v_ashrrev_i16_sdwa v3, v250, sext(v3) dst_sel:DWORD dst_unused:UNUSED_PAD src0_sel:DWORD src1_sel:BYTE_0
	s_min_i32 s8, s8, 8
	v_and_b32_e32 v4, 32, v4
	v_bfe_i32 v3, v3, 0, 16
	s_abs_i32 s10, s8
	v_add_lshl_u32 v212, v4, v3, 1
	v_cvt_f32_u32_e32 v3, s10
	s_sub_i32 s11, 0, s10
	s_andn2_b32 s3, s3, 63
	s_sub_i32 s2, s2, s3
	v_rcp_iflag_f32_e32 v3, v3
	s_abs_i32 s9, s2
	s_xor_b32 s3, s2, s8
	s_ashr_i32 s3, s3, 31
	v_mul_f32_e32 v3, 0x4f7ffffe, v3
	v_cvt_u32_f32_e32 v3, v3
	v_lshlrev_b32_e32 v5, 1, v236
	v_lshrrev_b32_e32 v6, 2, v236
	v_and_b32_e32 v5, 24, v5
	v_readfirstlane_b32 s14, v3
	s_mul_i32 s11, s11, s14
	s_mul_hi_u32 s11, s14, s11
	s_add_i32 s14, s14, s11
	s_mul_hi_u32 s11, s9, s14
	s_mul_i32 s14, s11, s10
	s_sub_i32 s9, s9, s14
	s_add_i32 s14, s11, 1
	s_sub_i32 s15, s9, s10
	s_cmp_ge_u32 s9, s10
	s_cselect_b32 s11, s14, s11
	s_cselect_b32 s9, s15, s9
	s_add_i32 s14, s11, 1
	s_cmp_ge_u32 s9, s10
	s_cselect_b32 s9, s14, s11
	s_xor_b32 s9, s9, s3
	s_sub_i32 s53, s9, s3
	s_mul_i32 s3, s53, s8
	s_sub_i32 s2, s2, s3
	s_add_i32 s52, s5, s2
	s_lshl_b32 s2, s52, 2
	s_add_i32 s2, s2, 0
	s_add_i32 s2, s2, 0x20000
	v_mov_b32_e32 v3, s2
	ds_read_b32 v3, v3
	v_and_b32_e32 v6, 4, v6
	v_or3_b32 v5, v7, v6, v5
	v_lshl_add_u32 v172, v5, 10, v212
	v_mov_b32_e32 v171, v35
	s_waitcnt lgkmcnt(0)
	v_readfirstlane_b32 s2, v3
	s_lshr_b32 s100, s2, 8
	s_and_b32 s2, s2, 0xff
	s_lshl_b32 s2, s2, 3
	s_add_i32 s8, s2, s53
	s_lshl_b32 s2, s52, 8
	s_lshl_b32 s100, s100, 8
	s_add_i32 s2, s2, s100
	v_add_u32_e32 v4, s2, v1
	v_ashrrev_i32_e32 v5, 31, v4
	v_lshl_add_u64 v[4:5], v[4:5], 2, s[28:29]
	global_load_dword v3, v[4:5], off
	v_add_u32_e32 v4, s2, v236
	v_ashrrev_i32_e32 v5, 31, v4
	v_lshl_add_u64 v[4:5], v[4:5], 2, s[28:29]
	s_bitset1_b32 s2, 7
	s_ashr_i32 s9, s8, 31
	v_mov_b32_e32 v173, v35
	s_waitcnt vmcnt(0)
	v_min_u32_e32 v3, 0x43ff, v3
	v_lshl_add_u32 v174, v3, 10, v219
	global_load_dword v3, v[4:5], off
	v_add_u32_e32 v4, s2, v1
	v_ashrrev_i32_e32 v5, 31, v4
	v_lshl_add_u64 v[4:5], v[4:5], 2, s[28:29]
	s_waitcnt vmcnt(0)
	v_min_u32_e32 v3, 0x43ff, v3
	v_lshl_add_u32 v176, v3, 10, v212
	global_load_dword v3, v[4:5], off
	v_add_u32_e32 v4, s2, v236
	v_ashrrev_i32_e32 v5, 31, v4
	v_lshl_add_u64 v[4:5], v[4:5], 2, s[28:29]
	s_lshl_b64 s[2:3], s[8:9], 18
	s_add_u32 s10, s22, s2
	s_addc_u32 s11, s23, s3
	s_add_i32 s9, s25, 0
	s_add_i32 m0, s9, 0x10000
	s_add_i32 s26, s9, 0x2000
	global_load_lds_dwordx4 v170, s[10:11]
	s_add_i32 m0, s9, 0x12000
	s_add_u32 s2, s10, 0x20000
	global_load_lds_dwordx4 v172, s[10:11]
	s_mov_b32 m0, s9
	s_addc_u32 s3, s11, 0
	global_load_lds_dwordx4 v174, s[6:7]
	s_mov_b32 m0, s26
	s_add_i32 s27, s9, 0x4000
	global_load_lds_dwordx4 v176, s[6:7]
	s_add_i32 m0, s9, 0x14000
	s_add_i32 s34, s9, 0x6000
	global_load_lds_dwordx4 v170, s[2:3]
	s_add_i32 m0, s9, 0x16000
	v_lshl_add_u64 v[6:7], s[10:11], 0, v[172:173]
	global_load_lds_dwordx4 v172, s[2:3]
	s_mov_b32 m0, s27
	s_cmp_lg_u32 s1, 1
	s_waitcnt vmcnt(0)
	v_min_u32_e32 v3, 0x43ff, v3
	v_lshl_add_u32 v178, v3, 10, v219
	global_load_dword v3, v[4:5], off
	v_lshl_add_u64 v[4:5], s[10:11], 0, v[170:171]
	global_load_lds_dwordx4 v178, s[6:7]
	s_mov_b32 m0, s34
	s_waitcnt vmcnt(0)
	v_min_u32_e32 v3, 0x43ff, v3
	v_lshl_add_u32 v180, v3, 10, v212
	global_load_lds_dwordx4 v180, s[6:7]
	s_cbranch_scc1 .LBB0_1580
	s_barrier

.LBB0_1581:
	s_add_i32 s49, s49, 1
	s_mul_i32 s0, s49, s76
	s_mul_hi_u32 s1, s49, s95
	s_add_i32 s1, s1, s0
	s_mul_i32 s0, s49, s95
	s_add_u32 s0, s0, s97
	s_addc_u32 s1, s1, s91
	v_mov_b64_e32 v[2:3], s[4:5]
	v_cmp_ge_i64_e64 s[38:39], s[0:1], v[2:3]
	v_cmp_lt_i64_e64 s[2:3], s[0:1], v[2:3]
	s_and_b64 vcc, exec, s[38:39]
	s_cbranch_vccnz .LBB0_1583
	s_ashr_i32 s1, s0, 31
	s_lshr_b32 s1, s1, 29
	s_add_i32 s1, s0, s1
	s_ashr_i32 s14, s1, 3
	s_and_b32 s1, s1, -8
	s_sub_i32 s0, s0, s1
	s_cmp_lt_i32 s0, 0
	s_cselect_b32 s1, s24, s18
	s_mul_i32 s0, s1, s0
	s_add_i32 s0, s0, s14
	s_ashr_i32 s1, s0, 31
	s_lshr_b32 s1, s1, 26
	s_add_i32 s1, s0, s1
	s_ashr_i32 s14, s1, 6
	s_lshl_b32 s14, s14, 3
	s_sub_i32 s15, s18, s14
	s_min_i32 s15, s15, 8
	s_abs_i32 s44, s15
	v_cvt_f32_u32_e32 v2, s44
	s_sub_i32 s46, 0, s44
	s_andn2_b32 s1, s1, 63
	s_sub_i32 s0, s0, s1
	v_rcp_iflag_f32_e32 v2, v2
	s_abs_i32 s1, s0
	s_xor_b32 s45, s0, s15
	s_ashr_i32 s45, s45, 31
	v_mul_f32_e32 v2, 0x4f7ffffe, v2
	v_cvt_u32_f32_e32 v2, v2
	s_nop 0
	v_readfirstlane_b32 s47, v2
	s_mul_i32 s46, s46, s47
	s_mul_hi_u32 s46, s47, s46
	s_add_i32 s47, s47, s46
	s_mul_hi_u32 s46, s1, s47
	s_mul_i32 s47, s46, s44
	s_sub_i32 s1, s1, s47
	s_add_i32 s50, s46, 1
	s_sub_i32 s47, s1, s44
	s_cmp_ge_u32 s1, s44
	s_cselect_b32 s46, s50, s46
	s_cselect_b32 s1, s47, s1
	s_add_i32 s47, s46, 1
	s_cmp_ge_u32 s1, s44
	s_cselect_b32 s1, s47, s46
	s_xor_b32 s1, s1, s45
	s_sub_i32 s50, s1, s45
	s_mul_i32 s1, s50, s15
	s_sub_i32 s0, s0, s1
	s_add_i32 s51, s0, s14
	s_lshl_b32 s0, s51, 2
	s_add_i32 s0, s0, 0
	s_add_i32 s0, s0, 0x20000
	v_mov_b32_e32 v2, s0
	ds_read_b32 v2, v2
	s_waitcnt lgkmcnt(0)
	v_readfirstlane_b32 s0, v2
	s_lshr_b32 s100, s0, 8
	s_and_b32 s0, s0, 0xff
	s_lshl_b32 s0, s0, 3
	s_add_i32 s44, s0, s50
.LBB0_1583:
	s_andn2_b64 vcc, exec, s[2:3]
	v_mov_b32_e32 v215, v174
	v_mov_b32_e32 v216, v176
	v_mov_b32_e32 v217, v178
	v_mov_b32_e32 v218, v180
	s_cbranch_vccnz .LBB0_1585
	s_lshl_b32 s0, s51, 8
	s_lshl_b32 s101, s100, 8
	s_add_i32 s0, s0, s101
	v_add_u32_e32 v2, s0, v1
	v_ashrrev_i32_e32 v3, 31, v2
	v_lshl_add_u64 v[2:3], v[2:3], 2, s[28:29]
	global_load_dword v68, v[2:3], off
	v_add_u32_e32 v2, s0, v236
	v_ashrrev_i32_e32 v3, 31, v2
	v_lshl_add_u64 v[2:3], v[2:3], 2, s[28:29]
	global_load_dword v69, v[2:3], off
	s_bitset1_b32 s0, 7
	v_add_u32_e32 v2, s0, v1
	v_ashrrev_i32_e32 v3, 31, v2
	v_lshl_add_u64 v[2:3], v[2:3], 2, s[28:29]
	global_load_dword v70, v[2:3], off
	v_add_u32_e32 v2, s0, v236
	v_ashrrev_i32_e32 v3, 31, v2
	v_lshl_add_u64 v[2:3], v[2:3], 2, s[28:29]
	global_load_dword v71, v[2:3], off
	s_waitcnt vmcnt(0)
	v_min_u32_e32 v68, 0x43ff, v68
	v_min_u32_e32 v69, 0x43ff, v69
	v_min_u32_e32 v70, 0x43ff, v70
	v_min_u32_e32 v71, 0x43ff, v71
	v_lshl_add_u32 v215, v68, 10, v219
	v_lshl_add_u32 v216, v69, 10, v212
	v_lshl_add_u32 v217, v70, 10, v219
	v_lshl_add_u32 v218, v71, 10, v212

.LBB0_1658:
	v_mov_b32_e32 v4, s66
	ds_read2_b32 v[4:5], v4 offset1:1
	s_waitcnt lgkmcnt(0)
	v_ashrrev_i32_e32 v4, 8, v4
	v_cmp_le_i32_e32 vcc, v4, v3
	v_ashrrev_i32_e32 v5, 8, v5
	s_nop 0
	v_cndmask_b32_e64 v4, 0, 1, vcc
	v_cmp_gt_i32_e32 vcc, v5, v3
	s_nop 1
	v_cndmask_b32_e32 v6, 2, v4, vcc
	v_mov_b32_e32 v4, s67
	ds_read2_b32 v[4:5], v4 offset1:1
	s_waitcnt lgkmcnt(0)
	v_ashrrev_i32_e32 v4, 8, v4
	v_cmp_gt_i32_e32 vcc, v4, v3
	v_ashrrev_i32_e32 v5, 8, v5
	s_nop 0
	v_cndmask_b32_e32 v4, 3, v6, vcc
	v_cmp_gt_i32_e32 vcc, v5, v3
	s_nop 1
	v_cndmask_b32_e32 v6, 4, v4, vcc
	v_mov_b32_e32 v4, s72
	ds_read2_b32 v[4:5], v4 offset1:1
	s_waitcnt lgkmcnt(0)
	v_ashrrev_i32_e32 v4, 8, v4
	v_cmp_gt_i32_e32 vcc, v4, v3
	v_ashrrev_i32_e32 v5, 8, v5
	s_nop 0
	v_cndmask_b32_e32 v4, 5, v6, vcc
	v_cmp_gt_i32_e32 vcc, v5, v3
	s_nop 1
	v_cndmask_b32_e32 v6, 6, v4, vcc
	v_mov_b32_e32 v4, s74
	ds_read2_b32 v[4:5], v4 offset1:1
	s_waitcnt lgkmcnt(0)
	v_ashrrev_i32_e32 v4, 8, v4
	v_cmp_gt_i32_e32 vcc, v4, v3
	v_ashrrev_i32_e32 v5, 8, v5
	s_nop 0
	v_cndmask_b32_e32 v4, 7, v6, vcc
	v_cmp_gt_i32_e32 vcc, v5, v3
	s_nop 1
	v_cndmask_b32_e32 v6, 8, v4, vcc
	v_mov_b32_e32 v4, s75
	ds_read2_b32 v[4:5], v4 offset1:1
	s_waitcnt lgkmcnt(0)
	v_ashrrev_i32_e32 v4, 8, v4
	v_cmp_gt_i32_e32 vcc, v4, v3
	v_ashrrev_i32_e32 v5, 8, v5
	s_nop 0
	v_cndmask_b32_e32 v4, 9, v6, vcc
	v_cmp_gt_i32_e32 vcc, v5, v3
	s_nop 1
	v_cndmask_b32_e32 v6, 10, v4, vcc
	v_mov_b32_e32 v4, s77
	ds_read2_b32 v[4:5], v4 offset1:1
	s_waitcnt lgkmcnt(0)
	v_ashrrev_i32_e32 v4, 8, v4
	v_cmp_gt_i32_e32 vcc, v4, v3
	v_ashrrev_i32_e32 v5, 8, v5
	s_nop 0
	v_cndmask_b32_e32 v4, 11, v6, vcc
	v_cmp_gt_i32_e32 vcc, v5, v3
	s_nop 1
	v_cndmask_b32_e32 v6, 12, v4, vcc
	v_mov_b32_e32 v4, s78
	ds_read2_b32 v[4:5], v4 offset1:1
	s_waitcnt lgkmcnt(0)
	v_ashrrev_i32_e32 v4, 8, v4
	v_cmp_gt_i32_e32 vcc, v4, v3
	v_ashrrev_i32_e32 v5, 8, v5
	s_nop 0
	v_cndmask_b32_e32 v4, 13, v6, vcc
	v_cmp_gt_i32_e32 vcc, v5, v3
	s_nop 1
	v_cndmask_b32_e32 v6, 14, v4, vcc
	v_mov_b32_e32 v4, s79
	ds_read2_b32 v[4:5], v4 offset1:1
	s_waitcnt lgkmcnt(0)
	v_ashrrev_i32_e32 v4, 8, v4
	v_cmp_gt_i32_e32 vcc, v4, v3
	v_ashrrev_i32_e32 v5, 8, v5
	s_nop 0
	v_cndmask_b32_e32 v4, 15, v6, vcc
	v_cmp_gt_i32_e32 vcc, v5, v3
	s_nop 1
	v_cndmask_b32_e32 v6, 16, v4, vcc
	v_mov_b32_e32 v4, s82
	ds_read2_b32 v[4:5], v4 offset1:1
	s_waitcnt lgkmcnt(0)
	v_ashrrev_i32_e32 v4, 8, v4
	v_cmp_gt_i32_e32 vcc, v4, v3
	v_ashrrev_i32_e32 v5, 8, v5
	s_nop 0
	v_cndmask_b32_e32 v4, 17, v6, vcc
	v_cmp_gt_i32_e32 vcc, v5, v3
	s_nop 1
	v_cndmask_b32_e32 v6, 18, v4, vcc
	v_mov_b32_e32 v4, s83
	ds_read2_b32 v[4:5], v4 offset1:1
	s_waitcnt lgkmcnt(0)
	v_ashrrev_i32_e32 v4, 8, v4
	v_cmp_gt_i32_e32 vcc, v4, v3
	v_ashrrev_i32_e32 v5, 8, v5
	s_nop 0
	v_cndmask_b32_e32 v4, 19, v6, vcc
	v_cmp_gt_i32_e32 vcc, v5, v3
	s_nop 1
	v_cndmask_b32_e32 v6, 20, v4, vcc
	v_mov_b32_e32 v4, s84
	ds_read2_b32 v[4:5], v4 offset1:1
	s_waitcnt lgkmcnt(0)
	v_ashrrev_i32_e32 v4, 8, v4
	v_cmp_gt_i32_e32 vcc, v4, v3
	v_ashrrev_i32_e32 v5, 8, v5
	s_nop 0
	v_cndmask_b32_e32 v4, 21, v6, vcc
	v_cmp_gt_i32_e32 vcc, v5, v3
	s_nop 1
	v_cndmask_b32_e32 v6, 22, v4, vcc
	v_mov_b32_e32 v4, s85
	ds_read2_b32 v[4:5], v4 offset1:1
	s_waitcnt lgkmcnt(0)
	v_ashrrev_i32_e32 v4, 8, v4
	v_cmp_gt_i32_e32 vcc, v4, v3
	v_ashrrev_i32_e32 v5, 8, v5
	s_nop 0
	v_cndmask_b32_e32 v4, 23, v6, vcc
	v_cmp_gt_i32_e32 vcc, v5, v3
	s_nop 1
	v_cndmask_b32_e32 v6, 24, v4, vcc
	v_mov_b32_e32 v4, s10
	ds_read2_b32 v[4:5], v4 offset1:1
	s_waitcnt lgkmcnt(0)
	v_ashrrev_i32_e32 v4, 8, v4
	v_cmp_gt_i32_e32 vcc, v4, v3
	v_ashrrev_i32_e32 v5, 8, v5
	s_nop 0
	v_cndmask_b32_e32 v4, 25, v6, vcc
	v_cmp_gt_i32_e32 vcc, v5, v3
	s_nop 1
	v_cndmask_b32_e32 v6, 26, v4, vcc
	v_mov_b32_e32 v4, s11
	ds_read2_b32 v[4:5], v4 offset1:1
	s_waitcnt lgkmcnt(0)
	v_ashrrev_i32_e32 v4, 8, v4
	v_cmp_gt_i32_e32 vcc, v4, v3
	v_ashrrev_i32_e32 v5, 8, v5
	s_nop 0
	v_cndmask_b32_e32 v4, 27, v6, vcc
	v_cmp_gt_i32_e32 vcc, v5, v3
	s_nop 1
	v_cndmask_b32_e32 v6, 28, v4, vcc
	v_mov_b32_e32 v4, s14
	ds_read2_b32 v[4:5], v4 offset1:1
	s_waitcnt lgkmcnt(0)
	v_ashrrev_i32_e32 v4, 8, v4
	v_cmp_gt_i32_e32 vcc, v4, v3
	v_ashrrev_i32_e32 v5, 8, v5
	s_nop 0
	v_cndmask_b32_e32 v4, 29, v6, vcc
	v_cmp_gt_i32_e32 vcc, v5, v3
	v_mov_b32_e32 v5, s65
	ds_read_b32 v5, v5
	v_cndmask_b32_e32 v4, 30, v4, vcc
	s_waitcnt lgkmcnt(0)
	v_ashrrev_i32_e32 v5, 8, v5
	v_cmp_gt_i32_e32 vcc, v5, v3
	v_add_u32_e32 v3, 0x200, v3
	s_nop 0
	v_cndmask_b32_e32 v4, 31, v4, vcc
	v_lshlrev_b32_e32 v5, 2, v4
	v_add_u32_e32 v5, 0x20840, v5
	ds_read_b32 v5, v5
	v_mul_u32_u24_e32 v6, 0x44, v4
	s_waitcnt lgkmcnt(0)
	v_ashrrev_i32_e32 v5, 8, v5
	v_sub_u32_e32 v6, v6, v5
	v_lshl_or_b32 v4, v6, 8, v4
	v_cmp_le_i32_e32 vcc, s24, v3
	ds_write_b32 v1, v4
	v_add_u32_e32 v1, 0x800, v1
	s_or_b64 s[4:5], vcc, s[4:5]
	s_andn2_b64 exec, exec, s[4:5]
	s_cbranch_execnz .LBB0_1658
.LBB0_1659:
	s_or_b64 exec, exec, s[2:3]
	s_lshl_b32 s4, s24, 2
	s_cmp_ge_i32 s97, s4
	v_readfirstlane_b32 s25, v2
	s_mov_b64 s[74:75], 0x40000
	s_mov_b64 s[78:79], 0x48000
	s_mov_b64 s[82:83], 0x50000
	s_mov_b64 s[84:85], 0x58000
	s_waitcnt lgkmcnt(0)
	s_barrier
	s_cbranch_scc1 .LBB0_1677
	v_ashrrev_i32_e32 v1, 31, v2
	v_lshrrev_b32_e32 v1, 26, v1
	v_add_u32_e32 v1, v2, v1
	v_readlane_b32 s0, v255, 37
	v_ashrrev_i32_e32 v4, 6, v1
	v_bfe_i32 v1, v2, 27, 1
	s_add_u32 s6, s16, 0x2bcec000
	v_readlane_b32 s1, v255, 38
	v_lshlrev_b32_e32 v3, 4, v2
	v_lshrrev_b32_e32 v1, 22, v1
	s_addc_u32 s7, s17, 0
	s_lshl_b64 s[0:1], s[0:1], 25
	v_add_u32_e32 v1, v3, v1
	s_add_u32 s0, s16, s0
	v_and_b32_e32 v1, 0xfffffc00, v1
	s_addc_u32 s1, s17, s1
	v_sub_u32_e32 v1, v3, v1
	s_add_u32 s26, s0, 0x60eec000
	v_lshrrev_b32_e32 v5, 4, v1
	s_addc_u32 s27, s1, 0
	v_bitop3_b32 v5, v5, v1, 32 bitop3:0x6c
	s_lshr_b32 s0, s24, 31
	v_ashrrev_i32_e32 v6, 31, v5
	s_add_i32 s0, s24, s0
	v_lshrrev_b32_e32 v6, 26, v6
	s_ashr_i32 s34, s0, 1
	s_lshr_b32 s0, s4, 29
	v_add_u32_e32 v6, v5, v6
	s_add_i32 s0, s4, s0
	v_ashrrev_i32_e32 v7, 6, v6
	v_and_b32_e32 v6, 0xc0, v6
	s_and_b32 s0, s0, -8
	v_sub_u32_e32 v5, v5, v6
	s_sub_i32 s35, s4, s0
	v_readlane_b32 s5, v254, 16
	v_lshlrev_b32_e32 v1, 3, v4
	v_lshlrev_b32_e32 v4, 5, v4
	v_ashrrev_i16_sdwa v5, v250, sext(v5) dst_sel:DWORD dst_unused:UNUSED_PAD src0_sel:DWORD src1_sel:BYTE_0
	s_add_i32 s36, s34, 1
	s_sub_i32 s3, s5, s35
	v_and_b32_e32 v4, 32, v4
	v_bfe_i32 v5, v5, 0, 16
	v_add_u32_e32 v3, 0x2000, v3
	s_mul_i32 s37, s36, s35
	s_ashr_i32 s0, s25, 6
	s_mul_i32 s3, s3, s34
	v_add_lshl_u32 v169, v4, v5, 1
	v_ashrrev_i32_e32 v4, 31, v3
	s_ashr_i32 s1, s25, 8
	s_lshl_b32 s44, s0, 10
	s_add_i32 s3, s3, s37
	v_lshrrev_b32_e32 v4, 22, v4
	s_mul_i32 s2, s36, s5
	s_cmp_lt_i32 s5, s35
	v_add_u32_e32 v4, v3, v4
	s_cselect_b32 s2, s2, s3
	v_readlane_b32 s3, v254, 17
	v_and_b32_e32 v1, -16, v1
	v_ashrrev_i32_e32 v4, 10, v4
	s_add_i32 s2, s2, s3
	v_add_u32_e32 v1, v7, v1
	v_mul_i32_i24_e32 v5, 0x400, v4
	s_ashr_i32 s3, s2, 31
	v_lshlrev_b32_e32 v6, 1, v1
	v_lshrrev_b32_e32 v8, 2, v1
	v_and_b32_e32 v7, 3, v7
	s_mov_b32 s18, 0x3fffe0
	v_sub_u32_e32 v3, v3, v5
	s_lshr_b32 s3, s3, 27
	v_and_b32_e32 v6, 24, v6
	v_and_b32_e32 v8, 4, v8
	v_and_or_b32 v7, v1, s18, v7
	v_lshrrev_b32_e32 v5, 4, v3
	s_add_i32 s3, s2, s3
	v_or3_b32 v6, v7, v8, v6
	v_bitop3_b32 v3, v5, v3, 32 bitop3:0x6c
	s_ashr_i32 s5, s3, 5
	v_lshl_add_u32 v170, v6, 10, v169
	v_ashrrev_i32_e32 v6, 31, v3
	s_lshl_b32 s5, s5, 3
	v_lshrrev_b32_e32 v6, 26, v6
	s_sub_i32 s8, s24, s5
	v_lshlrev_b32_e32 v5, 3, v4
	v_add_u32_e32 v6, v3, v6
	s_min_i32 s8, s8, 8
	v_and_b32_e32 v5, -16, v5
	v_ashrrev_i32_e32 v7, 6, v6
	s_abs_i32 s9, s8
	v_add_u32_e32 v210, v7, v5
	v_and_b32_e32 v5, 0xc0, v6
	v_cvt_f32_u32_e32 v6, s9
	s_sub_i32 s11, 0, s9
	s_andn2_b32 s3, s3, 31
	s_sub_i32 s2, s2, s3
	v_rcp_iflag_f32_e32 v6, v6
	s_abs_i32 s10, s2
	s_xor_b32 s3, s2, s8
	s_ashr_i32 s3, s3, 31
	v_mul_f32_e32 v6, 0x4f7ffffe, v6
	v_cvt_u32_f32_e32 v6, v6
	v_sub_u32_e32 v3, v3, v5
	v_lshlrev_b32_e32 v4, 5, v4
	v_ashrrev_i16_sdwa v3, v250, sext(v3) dst_sel:DWORD dst_unused:UNUSED_PAD src0_sel:DWORD src1_sel:BYTE_0
	v_readfirstlane_b32 s14, v6
	s_mul_i32 s11, s11, s14
	s_mul_hi_u32 s11, s14, s11
	s_add_i32 s14, s14, s11
	s_mul_hi_u32 s11, s10, s14
	s_mul_i32 s14, s11, s9
	s_sub_i32 s10, s10, s14
	s_add_i32 s14, s11, 1
	s_sub_i32 s15, s10, s9
	s_cmp_ge_u32 s10, s9
	s_cselect_b32 s11, s14, s11
	s_cselect_b32 s10, s15, s10
	s_add_i32 s14, s11, 1
	s_cmp_ge_u32 s10, s9
	s_cselect_b32 s9, s14, s11
	s_xor_b32 s9, s9, s3
	s_sub_i32 s56, s9, s3
	s_mul_i32 s3, s56, s8
	s_sub_i32 s2, s2, s3
	s_add_i32 s55, s5, s2
	s_lshl_b32 s2, s55, 2
	s_add_i32 s2, s2, 0
	s_add_i32 s2, s2, 0x20000
	v_mov_b32_e32 v6, s2
	ds_read_b32 v6, v6
	v_and_b32_e32 v4, 32, v4
	v_bfe_i32 v3, v3, 0, 16
	v_add_lshl_u32 v211, v4, v3, 1
	v_and_b32_e32 v7, 3, v7
	s_waitcnt lgkmcnt(0)
	v_readfirstlane_b32 s2, v6
	s_and_b32 s2, s2, 0xff
	s_lshl_b32 s2, s2, 2
	s_add_i32 s8, s2, s56
	s_lshl_b32 s2, s55, 8
	v_add_u32_e32 v3, s2, v1
	v_lshl_add_u32 v174, v3, 10, v169
	v_add_u32_e32 v3, s2, v210
	s_bitset1_b32 s2, 7
	v_lshl_add_u32 v176, v3, 10, v211
	v_add_u32_e32 v3, s2, v1
	s_ashr_i32 s9, s8, 31
	v_lshl_add_u32 v178, v3, 10, v169
	v_add_u32_e32 v3, s2, v210
	s_lshl_b64 s[2:3], s[8:9], 18
	v_lshlrev_b32_e32 v5, 1, v210
	v_lshrrev_b32_e32 v8, 2, v210
	v_and_or_b32 v7, v210, s18, v7
	s_add_u32 s18, s26, s2
	v_and_b32_e32 v5, 24, v5
	v_and_b32_e32 v8, 4, v8
	s_addc_u32 s19, s27, s3
	s_add_i32 s9, s44, 0
	v_or3_b32 v5, v7, v8, v5
	s_add_i32 m0, s9, 0x10000
	v_lshl_add_u32 v172, v5, 10, v211
	global_load_lds_dwordx4 v170, s[18:19]
	s_add_i32 m0, s9, 0x12000
	s_add_i32 s45, s9, 0x2000
	global_load_lds_dwordx4 v172, s[18:19]
	s_mov_b32 m0, s9
	s_add_u32 s2, s18, 0x20000
	global_load_lds_dwordx4 v174, s[6:7]
	s_mov_b32 m0, s45
	s_addc_u32 s3, s19, 0
	global_load_lds_dwordx4 v176, s[6:7]
	s_add_i32 m0, s9, 0x14000
	s_add_i32 s46, s9, 0x4000
	global_load_lds_dwordx4 v170, s[2:3]
	s_add_i32 m0, s9, 0x16000
	s_add_i32 s47, s9, 0x6000
	global_load_lds_dwordx4 v172, s[2:3]
	s_mov_b32 m0, s46
	v_lshl_add_u32 v180, v3, 10, v211
	global_load_lds_dwordx4 v178, s[6:7]
	s_mov_b32 m0, s47
	v_mov_b32_e32 v171, v35
	global_load_lds_dwordx4 v180, s[6:7]
	v_mov_b32_e32 v173, v35
	v_lshl_add_u64 v[6:7], s[18:19], 0, v[170:171]
	s_cmp_lg_u32 s1, 1
	v_lshl_add_u64 v[4:5], s[18:19], 0, v[172:173]
	s_cbranch_scc1 .LBB0_1662
	s_barrier
.LBB0_1662:
	v_readlane_b32 s2, v255, 37
	s_add_u32 s28, s16, 0x354ec000
	v_readlane_b32 s3, v255, 38
	v_readlane_b32 s60, v252, 48
	s_addc_u32 s29, s17, 0
	s_lshl_b64 s[2:3], s[2:3], 17
	v_readlane_b32 s66, v252, 54
	v_readlane_b32 s67, v252, 55
	s_add_u32 s48, s66, s2
	s_addc_u32 s49, s67, s3
	s_add_u32 s40, s16, 0xd818000
	s_addc_u32 s41, s17, 0
	s_add_u32 s42, s16, 0x2bcec080
	v_and_b32_e32 v3, 15, v2
	v_lshrrev_b32_e32 v8, 1, v2
	s_addc_u32 s43, s17, 0
	s_lshl_b32 s0, s0, 5
	v_and_b32_e32 v8, 24, v8
	v_lshlrev_b32_e32 v9, 6, v3
	v_lshlrev_b32_e32 v2, 2, v2
	s_and_b32 s2, s0, 0x60
	v_lshl_or_b32 v9, v8, 1, v9
	v_and_b32_e32 v2, 32, v2
	v_lshl_or_b32 v212, s1, 6, v3
	s_lshl_b32 s1, s1, 13
	s_lshl_b32 s0, s2, 7
	v_bitop3_b32 v10, v9, s1, v2 bitop3:0xde
	v_bitop3_b32 v213, s0, v9, v2 bitop3:0xf6
	s_add_i32 m0, s9, 0x18000
	v_lshl_add_u64 v[2:3], v[6:7], 0, s[20:21]
	v_mov_b32_e32 v175, v35
	s_ashr_i32 s5, s4, 31
	s_waitcnt vmcnt(4)
	s_barrier
	global_load_lds_dwordx4 v[2:3], off
	v_lshl_add_u64 v[2:3], v[4:5], 0, s[20:21]
	s_add_i32 m0, s9, 0x1a000
	s_add_i32 s50, s9, 0x8000
	s_add_i32 s51, s9, 0xa000
	v_mov_b32_e32 v177, v35
	global_load_lds_dwordx4 v[2:3], off
	v_lshl_add_u64 v[2:3], s[42:43], 0, v[174:175]
	s_mov_b32 m0, s50
	s_add_u32 s0, s18, 0x20080
	global_load_lds_dwordx4 v[2:3], off
	v_lshl_add_u64 v[2:3], s[42:43], 0, v[176:177]
	s_mov_b32 m0, s51
	s_addc_u32 s1, s19, 0
	global_load_lds_dwordx4 v[2:3], off
	s_add_i32 m0, s9, 0x1c000
	v_lshl_add_u64 v[2:3], s[0:1], 0, v[170:171]
	global_load_lds_dwordx4 v[2:3], off
	v_lshl_add_u64 v[2:3], s[0:1], 0, v[172:173]
	s_add_i32 m0, s9, 0x1e000
	v_or_b32_e32 v175, s2, v8
	global_load_lds_dwordx4 v[2:3], off
	s_waitcnt vmcnt(6)
	s_mov_b32 s52, 0
	v_add_u32_e32 v177, 0, v10
	v_readlane_b32 s61, v252, 49
	v_readlane_b32 s62, v252, 50
	v_readlane_b32 s63, v252, 51
	v_readlane_b32 s64, v252, 52
	v_readlane_b32 s65, v252, 53
	s_barrier

.LBB0_1668:
	s_ashr_i32 s0, s10, 3
	s_add_i32 s0, s14, s0
	s_ashr_i32 s1, s0, 31
	s_lshr_b32 s1, s1, 27
	s_add_i32 s1, s0, s1
	s_ashr_i32 s10, s1, 5
	s_lshl_b32 s10, s10, 3
	s_sub_i32 s11, s24, s10
	s_min_i32 s11, s11, 8
	s_abs_i32 s14, s11
	v_cvt_f32_u32_e32 v2, s14
	s_sub_i32 s22, 0, s14
	s_andn2_b32 s1, s1, 31
	s_sub_i32 s0, s0, s1
	v_rcp_iflag_f32_e32 v2, v2
	s_abs_i32 s1, s0
	s_xor_b32 s15, s0, s11
	s_ashr_i32 s15, s15, 31
	v_mul_f32_e32 v2, 0x4f7ffffe, v2
	v_cvt_u32_f32_e32 v2, v2
	s_nop 0
	v_readfirstlane_b32 s23, v2
	s_mul_i32 s22, s22, s23
	s_mul_hi_u32 s22, s23, s22
	s_add_i32 s23, s23, s22
	s_mul_hi_u32 s22, s1, s23
	s_mul_i32 s23, s22, s14
	s_sub_i32 s1, s1, s23
	s_add_i32 s53, s22, 1
	s_sub_i32 s23, s1, s14
	s_cmp_ge_u32 s1, s14
	s_cselect_b32 s22, s53, s22
	s_cselect_b32 s1, s23, s1
	s_add_i32 s23, s22, 1
	s_cmp_ge_u32 s1, s14
	s_cselect_b32 s1, s23, s22
	s_xor_b32 s1, s1, s15
	s_sub_i32 s53, s1, s15
	s_mul_i32 s1, s53, s11
	s_sub_i32 s0, s0, s1
	s_add_i32 s54, s10, s0
	s_lshl_b32 s0, s54, 2
	s_add_i32 s0, s0, 0
	s_add_i32 s0, s0, 0x20000
	v_mov_b32_e32 v2, s0
	ds_read_b32 v2, v2
	s_waitcnt lgkmcnt(0)
	v_readfirstlane_b32 s0, v2
	s_and_b32 s0, s0, 0xff
	s_lshl_b32 s0, s0, 2
	s_add_i32 s10, s0, s53

.LBB0_1672:
	s_add_u32 s18, s16, s2
	s_addc_u32 s19, s17, s3
	s_add_u32 s22, s18, 0x2bcec100
	s_addc_u32 s23, s19, 0
	s_add_u32 s59, s11, s2
	s_addc_u32 s60, s57, s3
	s_cmpk_eq_i32 s2, 0x300
	s_cselect_b64 vcc, -1, 0
	s_and_b64 s[18:19], vcc, exec
	s_cselect_b32 s23, s7, s23
	s_cselect_b32 s22, s6, s22
	s_cselect_b32 s19, s0, s60
	s_cselect_b32 s18, s1, s59
	s_add_i32 s60, 0, 0x10000
	v_add_u32_e32 v6, s60, v213
	ds_read_b128 v[10:13], v6
	ds_read_b128 v[14:17], v6 offset:1024
	ds_read_b128 v[2:5], v6 offset:2048
	ds_read_b128 v[6:9], v6 offset:3072
	v_cndmask_b32_e32 v34, v174, v214, vcc
	v_cndmask_b32_e32 v179, v178, v216, vcc
	v_cndmask_b32_e32 v190, v176, v215, vcc
	v_cndmask_b32_e32 v181, v180, v217, vcc
	v_lshl_add_u64 v[18:19], v[184:185], 0, s[2:3]
	s_add_i32 m0, s9, 0xc000
	ds_read_b128 v[192:195], v177
	ds_read_b128 v[196:199], v177 offset:1024
	ds_read_b128 v[218:221], v177 offset:2048
	ds_read_b128 v[222:225], v177 offset:3072
	ds_read_b128 v[226:229], v177 offset:4096
	ds_read_b128 v[230:233], v177 offset:5120
	ds_read_b128 v[242:245], v177 offset:6144
	ds_read_b128 v[246:249], v177 offset:7168
	global_load_lds_dwordx4 v[18:19], off
	v_lshl_add_u64 v[18:19], v[182:183], 0, s[2:3]
	s_add_i32 m0, s9, 0xe000
	s_nop 0
	global_load_lds_dwordx4 v[18:19], off
	s_waitcnt lgkmcnt(8)
	s_barrier
	s_waitcnt lgkmcnt(0)
	s_setprio 1
	s_waitcnt lgkmcnt(0)
	v_mfma_f32_16x16x128_f8f6f4 v[160:163], v[10:17], v[192:199], v[160:163]
	v_mfma_f32_16x16x128_f8f6f4 v[156:159], v[2:9], v[192:199], v[156:159]
	v_mfma_f32_16x16x128_f8f6f4 v[144:147], v[10:17], v[218:225], v[144:147]
	v_mfma_f32_16x16x128_f8f6f4 v[140:143], v[2:9], v[218:225], v[140:143]
	v_mfma_f32_16x16x128_f8f6f4 v[128:131], v[10:17], v[226:233], v[128:131]
	v_mfma_f32_16x16x128_f8f6f4 v[124:127], v[2:9], v[226:233], v[124:127]
	v_mfma_f32_16x16x128_f8f6f4 v[112:115], v[10:17], v[242:249], v[112:115]
	v_mfma_f32_16x16x128_f8f6f4 v[108:111], v[2:9], v[242:249], v[108:111]
	s_setprio 0
	s_barrier
	s_add_i32 s59, 0, 0x14000
	s_add_i32 s60, s60, s44
	v_add_u32_e32 v22, s59, v213
	v_lshl_add_u64 v[186:187], s[18:19], 0, v[170:171]
	s_mov_b32 m0, s60
	ds_read_b128 v[26:29], v22
	ds_read_b128 v[30:33], v22 offset:1024
	ds_read_b128 v[18:21], v22 offset:2048
	ds_read_b128 v[22:25], v22 offset:3072
	global_load_lds_dwordx4 v[186:187], off
	v_lshl_add_u64 v[188:189], s[18:19], 0, v[172:173]
	s_add_i32 m0, s60, 0x2000
	s_nop 0
	global_load_lds_dwordx4 v[188:189], off
	s_barrier
	s_waitcnt lgkmcnt(0)
	s_setprio 1
	s_waitcnt lgkmcnt(0)
	v_mfma_f32_16x16x128_f8f6f4 v[152:155], v[26:33], v[192:199], v[152:155]
	v_mfma_f32_16x16x128_f8f6f4 v[148:151], v[18:25], v[192:199], v[148:151]
	v_mfma_f32_16x16x128_f8f6f4 v[136:139], v[26:33], v[218:225], v[136:139]
	v_mfma_f32_16x16x128_f8f6f4 v[132:135], v[18:25], v[218:225], v[132:135]
	v_mfma_f32_16x16x128_f8f6f4 v[120:123], v[26:33], v[226:233], v[120:123]
	v_mfma_f32_16x16x128_f8f6f4 v[116:119], v[18:25], v[226:233], v[116:119]
	v_mfma_f32_16x16x128_f8f6f4 v[104:107], v[26:33], v[242:249], v[104:107]
	v_mfma_f32_16x16x128_f8f6f4 v[100:103], v[18:25], v[242:249], v[100:103]
	s_setprio 0
	s_mov_b32 m0, s9
	s_barrier
	ds_read_b128 v[218:221], v177 offset:16384
	ds_read_b128 v[222:225], v177 offset:17408
	ds_read_b128 v[226:229], v177 offset:18432
	ds_read_b128 v[230:233], v177 offset:19456
	ds_read_b128 v[242:245], v177 offset:20480
	ds_read_b128 v[246:249], v177 offset:21504
	ds_read_b128 v[234:237], v177 offset:22528
	ds_read_b128 v[238:241], v177 offset:23552
	global_load_lds_dwordx4 v34, s[22:23]
	s_mov_b32 m0, s45
	v_mov_b32_e32 v191, v35
	global_load_lds_dwordx4 v190, s[22:23]
	s_barrier
	s_waitcnt lgkmcnt(0)
	v_lshl_add_u64 v[192:193], s[22:23], 0, v[34:35]
	v_lshl_add_u64 v[190:191], s[22:23], 0, v[190:191]
	s_setprio 1
	s_waitcnt lgkmcnt(0)
	v_mfma_f32_16x16x128_f8f6f4 v[96:99], v[10:17], v[218:225], v[96:99]
	v_mfma_f32_16x16x128_f8f6f4 v[92:95], v[2:9], v[218:225], v[92:95]
	v_mfma_f32_16x16x128_f8f6f4 v[80:83], v[10:17], v[226:233], v[80:83]
	v_mfma_f32_16x16x128_f8f6f4 v[76:79], v[2:9], v[226:233], v[76:79]
	v_mfma_f32_16x16x128_f8f6f4 v[64:67], v[10:17], v[242:249], v[64:67]
	v_mfma_f32_16x16x128_f8f6f4 v[60:63], v[2:9], v[242:249], v[60:63]
	v_mfma_f32_16x16x128_f8f6f4 v[40:43], v[10:17], v[234:241], v[40:43]
	v_mfma_f32_16x16x128_f8f6f4 v[36:39], v[2:9], v[234:241], v[36:39]
	s_setprio 0
	s_barrier
	s_add_u32 s60, s18, 0x20000
	s_addc_u32 s61, s19, 0
	s_add_i32 s59, s59, s44
	v_lshl_add_u64 v[2:3], s[60:61], 0, v[170:171]
	s_mov_b32 m0, s59
	s_nop 0
	global_load_lds_dwordx4 v[2:3], off
	v_lshl_add_u64 v[2:3], s[60:61], 0, v[172:173]
	s_add_i32 m0, s59, 0x2000
	s_nop 0
	global_load_lds_dwordx4 v[2:3], off
	s_waitcnt vmcnt(6)
	s_barrier
	s_setprio 1
	v_mfma_f32_16x16x128_f8f6f4 v[88:91], v[26:33], v[218:225], v[88:91]
	v_mfma_f32_16x16x128_f8f6f4 v[84:87], v[18:25], v[218:225], v[84:87]
	v_mfma_f32_16x16x128_f8f6f4 v[72:75], v[26:33], v[226:233], v[72:75]
	v_mfma_f32_16x16x128_f8f6f4 v[68:71], v[18:25], v[226:233], v[68:71]
	v_mfma_f32_16x16x128_f8f6f4 v[56:59], v[26:33], v[242:249], v[56:59]
	v_mfma_f32_16x16x128_f8f6f4 v[52:55], v[18:25], v[242:249], v[52:55]
	v_mfma_f32_16x16x128_f8f6f4 v[48:51], v[26:33], v[234:241], v[48:51]
	v_mfma_f32_16x16x128_f8f6f4 v[44:47], v[18:25], v[234:241], v[44:47]
	s_setprio 0
	s_add_i32 s59, 0, 0x18000
	v_add_u32_e32 v14, s59, v213
	s_barrier
	ds_read_b128 v[2:5], v14
	ds_read_b128 v[6:9], v14 offset:1024
	ds_read_b128 v[10:13], v14 offset:2048
	ds_read_b128 v[14:17], v14 offset:3072
	s_mov_b32 m0, s46
	ds_read_b128 v[18:21], v177 offset:32768
	ds_read_b128 v[22:25], v177 offset:33792
	ds_read_b128 v[26:29], v177 offset:34816
	ds_read_b128 v[30:33], v177 offset:35840
	ds_read_b128 v[218:221], v177 offset:36864
	ds_read_b128 v[222:225], v177 offset:37888
	ds_read_b128 v[226:229], v177 offset:38912
	ds_read_b128 v[230:233], v177 offset:39936
	global_load_lds_dwordx4 v179, s[22:23]
	s_mov_b32 m0, s47
	s_nop 0
	global_load_lds_dwordx4 v181, s[22:23]
	s_waitcnt lgkmcnt(8)
	s_barrier
	s_waitcnt lgkmcnt(0)
	s_setprio 1
	s_waitcnt lgkmcnt(0)
	v_mfma_f32_16x16x128_f8f6f4 v[160:163], v[2:9], v[18:25], v[160:163]
	v_mfma_f32_16x16x128_f8f6f4 v[156:159], v[10:17], v[18:25], v[156:159]
	v_mfma_f32_16x16x128_f8f6f4 v[144:147], v[2:9], v[26:33], v[144:147]
	v_mfma_f32_16x16x128_f8f6f4 v[140:143], v[10:17], v[26:33], v[140:143]
	v_mfma_f32_16x16x128_f8f6f4 v[128:131], v[2:9], v[218:225], v[128:131]
	v_mfma_f32_16x16x128_f8f6f4 v[124:127], v[10:17], v[218:225], v[124:127]
	v_mfma_f32_16x16x128_f8f6f4 v[112:115], v[2:9], v[226:233], v[112:115]
	v_mfma_f32_16x16x128_f8f6f4 v[108:111], v[10:17], v[226:233], v[108:111]
	s_setprio 0
	s_barrier
	s_add_i32 s22, 0, 0x1c000
	s_add_i32 s23, s59, s44
	v_add_u32_e32 v34, s22, v213
	v_lshl_add_u64 v[186:187], v[186:187], 0, s[20:21]
	s_mov_b32 m0, s23
	ds_read_b128 v[234:237], v34
	ds_read_b128 v[238:241], v34 offset:1024
	ds_read_b128 v[242:245], v34 offset:2048
	ds_read_b128 v[246:249], v34 offset:3072
	global_load_lds_dwordx4 v[186:187], off
	v_lshl_add_u64 v[186:187], v[188:189], 0, s[20:21]
	s_add_i32 m0, s23, 0x2000
	s_nop 0
	global_load_lds_dwordx4 v[186:187], off
	s_barrier
	s_waitcnt lgkmcnt(0)
	s_setprio 1
	s_waitcnt lgkmcnt(0)
	v_mfma_f32_16x16x128_f8f6f4 v[152:155], v[234:241], v[18:25], v[152:155]
	v_mfma_f32_16x16x128_f8f6f4 v[148:151], v[242:249], v[18:25], v[148:151]
	v_mfma_f32_16x16x128_f8f6f4 v[136:139], v[234:241], v[26:33], v[136:139]
	v_mfma_f32_16x16x128_f8f6f4 v[132:135], v[242:249], v[26:33], v[132:135]
	v_mfma_f32_16x16x128_f8f6f4 v[120:123], v[234:241], v[218:225], v[120:123]
	v_mfma_f32_16x16x128_f8f6f4 v[116:119], v[242:249], v[218:225], v[116:119]
	v_mfma_f32_16x16x128_f8f6f4 v[104:107], v[234:241], v[226:233], v[104:107]
	v_mfma_f32_16x16x128_f8f6f4 v[100:103], v[242:249], v[226:233], v[100:103]
	s_setprio 0
	s_mov_b32 m0, s50
	v_lshl_add_u64 v[186:187], v[192:193], 0, s[20:21]
	s_barrier
	ds_read_b128 v[18:21], v177 offset:49152
	ds_read_b128 v[22:25], v177 offset:50176
	ds_read_b128 v[26:29], v177 offset:51200
	ds_read_b128 v[30:33], v177 offset:52224
	ds_read_b128 v[218:221], v177 offset:53248
	ds_read_b128 v[222:225], v177 offset:54272
	ds_read_b128 v[226:229], v177 offset:55296
	ds_read_b128 v[230:233], v177 offset:56320
	global_load_lds_dwordx4 v[186:187], off
	v_lshl_add_u64 v[186:187], v[190:191], 0, s[20:21]
	s_mov_b32 m0, s51
	s_nop 0
	global_load_lds_dwordx4 v[186:187], off
	s_barrier
	s_waitcnt lgkmcnt(0)
	s_setprio 1
	s_waitcnt lgkmcnt(0)
	v_mfma_f32_16x16x128_f8f6f4 v[96:99], v[2:9], v[18:25], v[96:99]
	v_mfma_f32_16x16x128_f8f6f4 v[92:95], v[10:17], v[18:25], v[92:95]
	v_mfma_f32_16x16x128_f8f6f4 v[80:83], v[2:9], v[26:33], v[80:83]
	v_mfma_f32_16x16x128_f8f6f4 v[76:79], v[10:17], v[26:33], v[76:79]
	v_mfma_f32_16x16x128_f8f6f4 v[64:67], v[2:9], v[218:225], v[64:67]
	v_mfma_f32_16x16x128_f8f6f4 v[60:63], v[10:17], v[218:225], v[60:63]
	v_mfma_f32_16x16x128_f8f6f4 v[40:43], v[2:9], v[226:233], v[40:43]
	v_mfma_f32_16x16x128_f8f6f4 v[36:39], v[10:17], v[226:233], v[36:39]
	s_setprio 0
	s_barrier
	s_add_u32 s18, s18, 0x20080
	s_addc_u32 s19, s19, 0
	s_add_i32 s22, s22, s44
	v_lshl_add_u64 v[2:3], s[18:19], 0, v[170:171]
	s_mov_b32 m0, s22
	s_nop 0
	global_load_lds_dwordx4 v[2:3], off
	v_lshl_add_u64 v[2:3], s[18:19], 0, v[172:173]
	s_add_i32 m0, s22, 0x2000
	s_nop 0
	global_load_lds_dwordx4 v[2:3], off
	s_waitcnt vmcnt(6)
	s_barrier
	s_setprio 1
	v_mfma_f32_16x16x128_f8f6f4 v[88:91], v[234:241], v[18:25], v[88:91]
	v_mfma_f32_16x16x128_f8f6f4 v[84:87], v[242:249], v[18:25], v[84:87]
	v_mfma_f32_16x16x128_f8f6f4 v[72:75], v[234:241], v[26:33], v[72:75]
	v_mfma_f32_16x16x128_f8f6f4 v[68:71], v[242:249], v[26:33], v[68:71]
	v_mfma_f32_16x16x128_f8f6f4 v[56:59], v[234:241], v[218:225], v[56:59]
	v_mfma_f32_16x16x128_f8f6f4 v[52:55], v[242:249], v[218:225], v[52:55]
	v_mfma_f32_16x16x128_f8f6f4 v[48:51], v[234:241], v[226:233], v[48:51]
	v_mfma_f32_16x16x128_f8f6f4 v[44:47], v[242:249], v[226:233], v[44:47]
	s_setprio 0
	s_add_i32 s58, s58, 2
	s_add_u32 s2, s2, 0x100
	s_addc_u32 s3, s3, 0
	s_cmp_gt_u32 s58, 5
	s_barrier
	s_cbranch_scc0 .LBB0_1672
	s_lshl_b32 s100, s55, 2
	s_add_i32 s100, s100, 0x20000
	v_mov_b32_e32 v20, s100
	ds_read_b32 v20, v20
	s_ashr_i32 s0, s8, 2
	s_ashr_i32 s1, s0, 31
	s_lshl_b64 s[0:1], s[0:1], 12
	v_lshl_or_b32 v18, s56, 8, v175
	s_add_u32 s0, s48, s0
	v_lshl_add_u32 v24, s55, 8, v212
	s_addc_u32 s1, s49, s1
	v_ashrrev_i32_e32 v19, 31, v18
	v_ashrrev_i32_e32 v25, 31, v24
	s_nop 15
	s_nop 15
	s_waitcnt lgkmcnt(0)
	v_readfirstlane_b32 s100, v20
	s_lshr_b32 s100, s100, 8
	s_lshl_b32 s100, s100, 10
	s_add_u32 s100, s40, s100
	s_addc_u32 s101, s41, 0
	v_lshl_add_u64 v[10:11], v[18:19], 2, s[0:1]
	v_lshl_add_u64 v[20:21], v[24:25], 2, s[100:101]
	global_load_dwordx4 v[6:9], v[10:11], off offset:16
	global_load_dwordx4 v[14:17], v[10:11], off
	global_load_dwordx4 v[2:5], v[10:11], off offset:528
	s_nop 0
	global_load_dwordx4 v[10:13], v[10:11], off offset:512
	v_lshlrev_b64 v[22:23], 11, v[24:25]
	global_load_dword v30, v[20:21], off
	global_load_dword v182, v[20:21], off offset:64
	global_load_dword v183, v[20:21], off offset:128
	global_load_dword v184, v[20:21], off offset:192
	global_load_dword v185, v[20:21], off offset:512
	global_load_dword v186, v[20:21], off offset:576
	global_load_dword v187, v[20:21], off offset:640
	global_load_dword v188, v[20:21], off offset:704
	v_lshl_add_u64 v[26:27], s[28:29], 0, v[22:23]
	v_lshlrev_b64 v[22:23], 1, v[18:19]
	v_lshl_add_u64 v[18:19], v[26:27], 0, v[22:23]
	v_mov_b32_e32 v180, v217
	v_mov_b32_e32 v178, v216
	v_mov_b32_e32 v176, v215
	v_mov_b32_e32 v174, v214
	s_mov_b32 s8, s10
	s_mov_b32 s56, s53
	s_mov_b32 s55, s54
	s_mov_b64 s[18:19], s[14:15]
	s_waitcnt vmcnt(0)
	v_pk_fma_f32 v[156:157], v[156:157], s[12:13], v[6:7] op_sel_hi:[1,0,1]
	v_pk_fma_f32 v[26:27], v[162:163], s[12:13], v[16:17] op_sel_hi:[1,0,1]
	v_pk_fma_f32 v[28:29], v[160:161], s[12:13], v[14:15] op_sel_hi:[1,0,1]
	v_pk_fma_f32 v[148:149], v[148:149], s[12:13], v[2:3] op_sel_hi:[1,0,1]
	v_pk_fma_f32 v[140:141], v[140:141], s[12:13], v[6:7] op_sel_hi:[1,0,1]
	v_pk_mul_f32 v[32:33], v[26:27], v[30:31] op_sel_hi:[1,0]
	v_pk_mul_f32 v[26:27], v[28:29], v[30:31] op_sel_hi:[1,0]
	v_pk_fma_f32 v[28:29], v[158:159], s[12:13], v[8:9] op_sel_hi:[1,0,1]
	v_cvt_pk_bf16_f32 v26, v26, v27
	v_pk_mul_f32 v[158:159], v[28:29], v[30:31] op_sel_hi:[1,0]
	v_pk_mul_f32 v[28:29], v[156:157], v[30:31] op_sel_hi:[1,0]
	v_cvt_pk_bf16_f32 v27, v32, v33
	v_cvt_pk_bf16_f32 v28, v28, v29
	v_cvt_pk_bf16_f32 v29, v158, v159
	global_store_dwordx4 v[18:19], v[26:29], off
	v_pk_fma_f32 v[132:133], v[132:133], s[12:13], v[2:3] op_sel_hi:[1,0,1]
	v_pk_fma_f32 v[124:125], v[124:125], s[12:13], v[6:7] op_sel_hi:[1,0,1]
	v_pk_fma_f32 v[26:27], v[154:155], s[12:13], v[12:13] op_sel_hi:[1,0,1]
	v_pk_fma_f32 v[28:29], v[152:153], s[12:13], v[10:11] op_sel_hi:[1,0,1]
	v_pk_mul_f32 v[32:33], v[26:27], v[30:31] op_sel_hi:[1,0]
	v_pk_mul_f32 v[26:27], v[28:29], v[30:31] op_sel_hi:[1,0]
	v_pk_fma_f32 v[28:29], v[150:151], s[12:13], v[4:5] op_sel_hi:[1,0,1]
	v_cvt_pk_bf16_f32 v26, v26, v27
	v_pk_mul_f32 v[150:151], v[28:29], v[30:31] op_sel_hi:[1,0]
	v_pk_mul_f32 v[28:29], v[148:149], v[30:31] op_sel_hi:[1,0]
	v_cvt_pk_bf16_f32 v27, v32, v33
	v_cvt_pk_bf16_f32 v28, v28, v29
	v_cvt_pk_bf16_f32 v29, v150, v151
	global_store_dwordx4 v[18:19], v[26:29], off offset:256
	v_pk_fma_f32 v[116:117], v[116:117], s[12:13], v[2:3] op_sel_hi:[1,0,1]
	s_nop 0
	v_or_b32_e32 v26, 16, v24
	v_ashrrev_i32_e32 v27, 31, v26
	v_lshl_add_u64 v[28:29], v[26:27], 2, s[40:41]
	v_mov_b32_e32 v30, v182
	v_lshlrev_b64 v[26:27], 11, v[26:27]
	v_lshl_add_u64 v[26:27], s[28:29], 0, v[26:27]
	v_lshl_add_u64 v[32:33], v[26:27], 0, v[22:23]
	v_pk_fma_f32 v[26:27], v[146:147], s[12:13], v[16:17] op_sel_hi:[1,0,1]
	v_pk_fma_f32 v[28:29], v[144:145], s[12:13], v[14:15] op_sel_hi:[1,0,1]
	v_pk_mul_f32 v[144:145], v[26:27], v[30:31] op_sel_hi:[1,0]
	v_pk_mul_f32 v[26:27], v[28:29], v[30:31] op_sel_hi:[1,0]
	v_pk_fma_f32 v[28:29], v[142:143], s[12:13], v[8:9] op_sel_hi:[1,0,1]
	v_cvt_pk_bf16_f32 v26, v26, v27
	v_pk_mul_f32 v[142:143], v[28:29], v[30:31] op_sel_hi:[1,0]
	v_pk_mul_f32 v[28:29], v[140:141], v[30:31] op_sel_hi:[1,0]
	v_cvt_pk_bf16_f32 v27, v144, v145
	v_cvt_pk_bf16_f32 v28, v28, v29
	v_cvt_pk_bf16_f32 v29, v142, v143
	global_store_dwordx4 v[32:33], v[26:29], off
	s_nop 1
	v_pk_fma_f32 v[26:27], v[138:139], s[12:13], v[12:13] op_sel_hi:[1,0,1]
	v_pk_fma_f32 v[28:29], v[136:137], s[12:13], v[10:11] op_sel_hi:[1,0,1]
	v_pk_mul_f32 v[136:137], v[26:27], v[30:31] op_sel_hi:[1,0]
	v_pk_mul_f32 v[26:27], v[28:29], v[30:31] op_sel_hi:[1,0]
	v_pk_fma_f32 v[28:29], v[134:135], s[12:13], v[4:5] op_sel_hi:[1,0,1]
	v_cvt_pk_bf16_f32 v26, v26, v27
	v_pk_mul_f32 v[134:135], v[28:29], v[30:31] op_sel_hi:[1,0]
	v_pk_mul_f32 v[28:29], v[132:133], v[30:31] op_sel_hi:[1,0]
	v_cvt_pk_bf16_f32 v27, v136, v137
	v_cvt_pk_bf16_f32 v28, v28, v29
	v_cvt_pk_bf16_f32 v29, v134, v135
	global_store_dwordx4 v[32:33], v[26:29], off offset:256
	s_nop 1
	v_or_b32_e32 v26, 32, v24
	v_ashrrev_i32_e32 v27, 31, v26
	v_lshl_add_u64 v[28:29], v[26:27], 2, s[40:41]
	v_mov_b32_e32 v30, v183
	v_lshlrev_b64 v[26:27], 11, v[26:27]
	v_lshl_add_u64 v[26:27], s[28:29], 0, v[26:27]
	v_lshl_add_u64 v[32:33], v[26:27], 0, v[22:23]
	v_pk_fma_f32 v[26:27], v[130:131], s[12:13], v[16:17] op_sel_hi:[1,0,1]
	v_pk_fma_f32 v[28:29], v[128:129], s[12:13], v[14:15] op_sel_hi:[1,0,1]
	v_or_b32_e32 v24, 48, v24
	v_ashrrev_i32_e32 v25, 31, v24
	v_pk_mul_f32 v[128:129], v[26:27], v[30:31] op_sel_hi:[1,0]
	v_pk_mul_f32 v[26:27], v[28:29], v[30:31] op_sel_hi:[1,0]
	v_pk_fma_f32 v[28:29], v[126:127], s[12:13], v[8:9] op_sel_hi:[1,0,1]
	v_cvt_pk_bf16_f32 v26, v26, v27
	v_pk_mul_f32 v[126:127], v[28:29], v[30:31] op_sel_hi:[1,0]
	v_pk_mul_f32 v[28:29], v[124:125], v[30:31] op_sel_hi:[1,0]
	v_cvt_pk_bf16_f32 v27, v128, v129
	v_cvt_pk_bf16_f32 v28, v28, v29
	v_cvt_pk_bf16_f32 v29, v126, v127
	global_store_dwordx4 v[32:33], v[26:29], off
	s_nop 1
	v_pk_fma_f32 v[26:27], v[122:123], s[12:13], v[12:13] op_sel_hi:[1,0,1]
	v_pk_fma_f32 v[28:29], v[120:121], s[12:13], v[10:11] op_sel_hi:[1,0,1]
	v_pk_mul_f32 v[120:121], v[26:27], v[30:31] op_sel_hi:[1,0]
	v_pk_mul_f32 v[26:27], v[28:29], v[30:31] op_sel_hi:[1,0]
	v_pk_fma_f32 v[28:29], v[118:119], s[12:13], v[4:5] op_sel_hi:[1,0,1]
	v_cvt_pk_bf16_f32 v26, v26, v27
	v_pk_mul_f32 v[118:119], v[28:29], v[30:31] op_sel_hi:[1,0]
	v_pk_mul_f32 v[28:29], v[116:117], v[30:31] op_sel_hi:[1,0]
	v_cvt_pk_bf16_f32 v27, v120, v121
	v_cvt_pk_bf16_f32 v28, v28, v29
	v_cvt_pk_bf16_f32 v29, v118, v119
	global_store_dwordx4 v[32:33], v[26:29], off offset:256
	v_pk_fma_f32 v[32:33], v[108:109], s[12:13], v[6:7] op_sel_hi:[1,0,1]
	s_nop 0
	v_lshl_add_u64 v[26:27], v[24:25], 2, s[40:41]
	v_mov_b32_e32 v26, v184
	v_lshlrev_b64 v[24:25], 11, v[24:25]
	v_lshl_add_u64 v[24:25], s[28:29], 0, v[24:25]
	v_lshl_add_u64 v[28:29], v[24:25], 0, v[22:23]
	v_pk_fma_f32 v[22:23], v[114:115], s[12:13], v[16:17] op_sel_hi:[1,0,1]
	v_pk_fma_f32 v[24:25], v[112:113], s[12:13], v[14:15] op_sel_hi:[1,0,1]
	v_pk_mul_f32 v[30:31], v[22:23], v[26:27] op_sel_hi:[1,0]
	v_pk_mul_f32 v[22:23], v[24:25], v[26:27] op_sel_hi:[1,0]
	v_pk_fma_f32 v[24:25], v[110:111], s[12:13], v[8:9] op_sel_hi:[1,0,1]
	v_cvt_pk_bf16_f32 v22, v22, v23
	v_pk_mul_f32 v[108:109], v[24:25], v[26:27] op_sel_hi:[1,0]
	v_pk_mul_f32 v[24:25], v[32:33], v[26:27] op_sel_hi:[1,0]
	v_cvt_pk_bf16_f32 v23, v30, v31
	v_cvt_pk_bf16_f32 v24, v24, v25
	v_cvt_pk_bf16_f32 v25, v108, v109
	global_store_dwordx4 v[28:29], v[22:25], off
	v_pk_fma_f32 v[32:33], v[100:101], s[12:13], v[2:3] op_sel_hi:[1,0,1]
	s_nop 0
	v_pk_fma_f32 v[22:23], v[106:107], s[12:13], v[12:13] op_sel_hi:[1,0,1]
	v_pk_fma_f32 v[24:25], v[104:105], s[12:13], v[10:11] op_sel_hi:[1,0,1]
	v_pk_mul_f32 v[30:31], v[22:23], v[26:27] op_sel_hi:[1,0]
	v_pk_mul_f32 v[22:23], v[24:25], v[26:27] op_sel_hi:[1,0]
	v_pk_fma_f32 v[24:25], v[102:103], s[12:13], v[4:5] op_sel_hi:[1,0,1]
	v_cvt_pk_bf16_f32 v22, v22, v23
	v_pk_mul_f32 v[100:101], v[24:25], v[26:27] op_sel_hi:[1,0]
	v_pk_mul_f32 v[24:25], v[32:33], v[26:27] op_sel_hi:[1,0]
	v_cvt_pk_bf16_f32 v23, v30, v31
	v_cvt_pk_bf16_f32 v24, v24, v25
	v_cvt_pk_bf16_f32 v25, v100, v101
	global_store_dwordx4 v[28:29], v[22:25], off offset:256
	v_mov_b32_e32 v26, v185
	v_pk_fma_f32 v[32:33], v[92:93], s[12:13], v[6:7] op_sel_hi:[1,0,1]
	v_pk_fma_f32 v[22:23], v[98:99], s[12:13], v[16:17] op_sel_hi:[1,0,1]
	v_pk_fma_f32 v[24:25], v[96:97], s[12:13], v[14:15] op_sel_hi:[1,0,1]
	v_lshl_add_u64 v[28:29], v[18:19], 0, s[74:75]
	v_pk_mul_f32 v[30:31], v[22:23], v[26:27] op_sel_hi:[1,0]
	v_pk_mul_f32 v[22:23], v[24:25], v[26:27] op_sel_hi:[1,0]
	v_pk_fma_f32 v[24:25], v[94:95], s[12:13], v[8:9] op_sel_hi:[1,0,1]
	v_cvt_pk_bf16_f32 v22, v22, v23
	v_pk_mul_f32 v[92:93], v[24:25], v[26:27] op_sel_hi:[1,0]
	v_pk_mul_f32 v[24:25], v[32:33], v[26:27] op_sel_hi:[1,0]
	v_cvt_pk_bf16_f32 v23, v30, v31
	v_add_co_u32_e32 v30, vcc, s68, v18
	v_cvt_pk_bf16_f32 v24, v24, v25
	v_cvt_pk_bf16_f32 v25, v92, v93
	v_addc_co_u32_e32 v31, vcc, 0, v19, vcc
	global_store_dwordx4 v[30:31], v[22:25], off
	v_pk_fma_f32 v[32:33], v[84:85], s[12:13], v[2:3] op_sel_hi:[1,0,1]
	s_nop 0
	v_pk_fma_f32 v[22:23], v[90:91], s[12:13], v[12:13] op_sel_hi:[1,0,1]
	v_pk_fma_f32 v[24:25], v[88:89], s[12:13], v[10:11] op_sel_hi:[1,0,1]
	v_pk_mul_f32 v[30:31], v[22:23], v[26:27] op_sel_hi:[1,0]
	v_pk_mul_f32 v[22:23], v[24:25], v[26:27] op_sel_hi:[1,0]
	v_pk_fma_f32 v[24:25], v[86:87], s[12:13], v[4:5] op_sel_hi:[1,0,1]
	v_cvt_pk_bf16_f32 v22, v22, v23
	v_pk_mul_f32 v[84:85], v[24:25], v[26:27] op_sel_hi:[1,0]
	v_pk_mul_f32 v[24:25], v[32:33], v[26:27] op_sel_hi:[1,0]
	v_cvt_pk_bf16_f32 v23, v30, v31
	v_cvt_pk_bf16_f32 v24, v24, v25
	v_cvt_pk_bf16_f32 v25, v84, v85
	global_store_dwordx4 v[28:29], v[22:25], off offset:256
	v_mov_b32_e32 v26, v186
	v_pk_fma_f32 v[32:33], v[76:77], s[12:13], v[6:7] op_sel_hi:[1,0,1]
	v_pk_fma_f32 v[22:23], v[82:83], s[12:13], v[16:17] op_sel_hi:[1,0,1]
	v_pk_fma_f32 v[24:25], v[80:81], s[12:13], v[14:15] op_sel_hi:[1,0,1]
	v_lshl_add_u64 v[28:29], v[18:19], 0, s[78:79]
	v_pk_mul_f32 v[30:31], v[22:23], v[26:27] op_sel_hi:[1,0]
	v_pk_mul_f32 v[22:23], v[24:25], v[26:27] op_sel_hi:[1,0]
	v_pk_fma_f32 v[24:25], v[78:79], s[12:13], v[8:9] op_sel_hi:[1,0,1]
	v_cvt_pk_bf16_f32 v22, v22, v23
	v_pk_mul_f32 v[76:77], v[24:25], v[26:27] op_sel_hi:[1,0]
	v_pk_mul_f32 v[24:25], v[32:33], v[26:27] op_sel_hi:[1,0]
	v_cvt_pk_bf16_f32 v23, v30, v31
	v_add_co_u32_e32 v30, vcc, s69, v18
	v_cvt_pk_bf16_f32 v24, v24, v25
	v_cvt_pk_bf16_f32 v25, v76, v77
	v_addc_co_u32_e32 v31, vcc, 0, v19, vcc
	global_store_dwordx4 v[30:31], v[22:25], off
	v_pk_fma_f32 v[32:33], v[68:69], s[12:13], v[2:3] op_sel_hi:[1,0,1]
	s_nop 0
	v_pk_fma_f32 v[22:23], v[74:75], s[12:13], v[12:13] op_sel_hi:[1,0,1]
	v_pk_fma_f32 v[24:25], v[72:73], s[12:13], v[10:11] op_sel_hi:[1,0,1]
	v_pk_mul_f32 v[30:31], v[22:23], v[26:27] op_sel_hi:[1,0]
	v_pk_mul_f32 v[22:23], v[24:25], v[26:27] op_sel_hi:[1,0]
	v_pk_fma_f32 v[24:25], v[70:71], s[12:13], v[4:5] op_sel_hi:[1,0,1]
	v_cvt_pk_bf16_f32 v22, v22, v23
	v_pk_mul_f32 v[68:69], v[24:25], v[26:27] op_sel_hi:[1,0]
	v_pk_mul_f32 v[24:25], v[32:33], v[26:27] op_sel_hi:[1,0]
	v_cvt_pk_bf16_f32 v23, v30, v31
	v_cvt_pk_bf16_f32 v24, v24, v25
	v_cvt_pk_bf16_f32 v25, v68, v69
	global_store_dwordx4 v[28:29], v[22:25], off offset:256
	v_mov_b32_e32 v26, v187
	v_pk_fma_f32 v[32:33], v[60:61], s[12:13], v[6:7] op_sel_hi:[1,0,1]
	v_pk_fma_f32 v[22:23], v[66:67], s[12:13], v[16:17] op_sel_hi:[1,0,1]
	v_pk_fma_f32 v[24:25], v[64:65], s[12:13], v[14:15] op_sel_hi:[1,0,1]
	v_lshl_add_u64 v[28:29], v[18:19], 0, s[82:83]
	v_pk_fma_f32 v[14:15], v[40:41], s[12:13], v[14:15] op_sel_hi:[1,0,1]
	v_pk_fma_f32 v[16:17], v[42:43], s[12:13], v[16:17] op_sel_hi:[1,0,1]
	v_pk_fma_f32 v[6:7], v[36:37], s[12:13], v[6:7] op_sel_hi:[1,0,1]
	v_pk_mul_f32 v[30:31], v[22:23], v[26:27] op_sel_hi:[1,0]
	v_pk_mul_f32 v[22:23], v[24:25], v[26:27] op_sel_hi:[1,0]
	v_pk_fma_f32 v[24:25], v[62:63], s[12:13], v[8:9] op_sel_hi:[1,0,1]
	v_cvt_pk_bf16_f32 v22, v22, v23
	v_pk_mul_f32 v[60:61], v[24:25], v[26:27] op_sel_hi:[1,0]
	v_pk_mul_f32 v[24:25], v[32:33], v[26:27] op_sel_hi:[1,0]
	v_cvt_pk_bf16_f32 v23, v30, v31
	v_add_co_u32_e32 v30, vcc, s70, v18
	v_cvt_pk_bf16_f32 v24, v24, v25
	v_cvt_pk_bf16_f32 v25, v60, v61
	v_addc_co_u32_e32 v31, vcc, 0, v19, vcc
	global_store_dwordx4 v[30:31], v[22:25], off
	v_pk_fma_f32 v[32:33], v[52:53], s[12:13], v[2:3] op_sel_hi:[1,0,1]
	v_pk_fma_f32 v[8:9], v[38:39], s[12:13], v[8:9] op_sel_hi:[1,0,1]
	v_pk_fma_f32 v[22:23], v[58:59], s[12:13], v[12:13] op_sel_hi:[1,0,1]
	v_pk_fma_f32 v[24:25], v[56:57], s[12:13], v[10:11] op_sel_hi:[1,0,1]
	v_pk_mul_f32 v[30:31], v[22:23], v[26:27] op_sel_hi:[1,0]
	v_pk_mul_f32 v[22:23], v[24:25], v[26:27] op_sel_hi:[1,0]
	v_pk_fma_f32 v[24:25], v[54:55], s[12:13], v[4:5] op_sel_hi:[1,0,1]
	v_cvt_pk_bf16_f32 v22, v22, v23
	v_pk_mul_f32 v[52:53], v[24:25], v[26:27] op_sel_hi:[1,0]
	v_pk_mul_f32 v[24:25], v[32:33], v[26:27] op_sel_hi:[1,0]
	v_cvt_pk_bf16_f32 v23, v30, v31
	v_cvt_pk_bf16_f32 v24, v24, v25
	v_cvt_pk_bf16_f32 v25, v52, v53
	global_store_dwordx4 v[28:29], v[22:25], off offset:256
	v_mov_b32_e32 v20, v188
	v_pk_fma_f32 v[4:5], v[46:47], s[12:13], v[4:5] op_sel_hi:[1,0,1]
	v_pk_fma_f32 v[2:3], v[44:45], s[12:13], v[2:3] op_sel_hi:[1,0,1]
	v_lshl_add_u64 v[22:23], v[18:19], 0, s[84:85]
	v_pk_mul_f32 v[14:15], v[14:15], v[20:21] op_sel_hi:[1,0]
	v_pk_mul_f32 v[16:17], v[16:17], v[20:21] op_sel_hi:[1,0]
	v_pk_mul_f32 v[24:25], v[8:9], v[20:21] op_sel_hi:[1,0]
	v_pk_mul_f32 v[8:9], v[6:7], v[20:21] op_sel_hi:[1,0]
	v_cvt_pk_bf16_f32 v6, v14, v15
	v_add_co_u32_e32 v14, vcc, s71, v18
	v_cvt_pk_bf16_f32 v7, v16, v17
	v_cvt_pk_bf16_f32 v8, v8, v9
	v_cvt_pk_bf16_f32 v9, v24, v25
	v_addc_co_u32_e32 v15, vcc, 0, v19, vcc
	global_store_dwordx4 v[14:15], v[6:9], off
	s_and_b64 vcc, exec, s[38:39]
	s_nop 0
	v_pk_fma_f32 v[6:7], v[50:51], s[12:13], v[12:13] op_sel_hi:[1,0,1]
	v_pk_fma_f32 v[8:9], v[48:49], s[12:13], v[10:11] op_sel_hi:[1,0,1]
	v_pk_mul_f32 v[6:7], v[6:7], v[20:21] op_sel_hi:[1,0]
	v_pk_mul_f32 v[8:9], v[8:9], v[20:21] op_sel_hi:[1,0]
	v_pk_mul_f32 v[10:11], v[4:5], v[20:21] op_sel_hi:[1,0]
	v_pk_mul_f32 v[4:5], v[2:3], v[20:21] op_sel_hi:[1,0]
	v_cvt_pk_bf16_f32 v2, v8, v9
	v_cvt_pk_bf16_f32 v3, v6, v7
	v_cvt_pk_bf16_f32 v4, v4, v5
	v_cvt_pk_bf16_f32 v5, v10, v11
	global_store_dwordx4 v[22:23], v[2:5], off offset:256
	s_cbranch_vccz .LBB0_1663
	s_waitcnt vmcnt(0)
	s_cmpk_gt_u32 s25, 0xff
	v_readlane_b32 s52, v255, 32
	s_cbranch_scc1 .LBB0_1676
	s_barrier

	.amdhsa_kernel _ZN2mk3fwdENS_4ArgsE
		.amdhsa_group_segment_fixed_size 0
		.amdhsa_private_segment_fixed_size 0
		.amdhsa_kernarg_size 576
		.amdhsa_user_sgpr_count 2
		.amdhsa_user_sgpr_dispatch_ptr 0
		.amdhsa_user_sgpr_queue_ptr 0
		.amdhsa_user_sgpr_kernarg_segment_ptr 1
		.amdhsa_user_sgpr_dispatch_id 0
		.amdhsa_user_sgpr_kernarg_preload_length 0
		.amdhsa_user_sgpr_kernarg_preload_offset 0
		.amdhsa_user_sgpr_private_segment_size 0
		.amdhsa_uses_dynamic_stack 0
		.amdhsa_enable_private_segment 0
		.amdhsa_system_sgpr_workgroup_id_x 1
		.amdhsa_system_sgpr_workgroup_id_y 0
		.amdhsa_system_sgpr_workgroup_id_z 0
		.amdhsa_system_sgpr_workgroup_info 0
		.amdhsa_system_vgpr_workitem_id 0
		.amdhsa_next_free_vgpr 256
		.amdhsa_next_free_sgpr 102
		.amdhsa_accum_offset 256
		.amdhsa_reserve_vcc 1
		.amdhsa_float_round_mode_32 0
		.amdhsa_float_round_mode_16_64 0
		.amdhsa_float_denorm_mode_32 3
		.amdhsa_float_denorm_mode_16_64 3
		.amdhsa_dx10_clamp 1
		.amdhsa_ieee_mode 1
		.amdhsa_fp16_overflow 0
		.amdhsa_tg_split 0
		.amdhsa_exception_fp_ieee_invalid_op 0
		.amdhsa_exception_fp_denorm_src 0
		.amdhsa_exception_fp_ieee_div_zero 0
		.amdhsa_exception_fp_ieee_overflow 0
		.amdhsa_exception_fp_ieee_underflow 0
		.amdhsa_exception_fp_ieee_inexact 0
		.amdhsa_exception_int_div_zero 0
	.end_amdhsa_kernel

amdhsa.kernels:
  - .agpr_count:     0
    .args:
      - .offset:         0
        .size:           320
        .value_kind:     by_value
      - .offset:         320
        .size:           4
        .value_kind:     hidden_block_count_x
      - .offset:         324
        .size:           4
        .value_kind:     hidden_block_count_y
      - .offset:         328
        .size:           4
        .value_kind:     hidden_block_count_z
      - .offset:         332
        .size:           2
        .value_kind:     hidden_group_size_x
      - .offset:         334
        .size:           2
        .value_kind:     hidden_group_size_y
      - .offset:         336
        .size:           2
        .value_kind:     hidden_group_size_z
      - .offset:         338
        .size:           2
        .value_kind:     hidden_remainder_x
      - .offset:         340
        .size:           2
        .value_kind:     hidden_remainder_y
      - .offset:         342
        .size:           2
        .value_kind:     hidden_remainder_z
      - .offset:         360
        .size:           8
        .value_kind:     hidden_global_offset_x
      - .offset:         368
        .size:           8
        .value_kind:     hidden_global_offset_y
      - .offset:         376
        .size:           8
        .value_kind:     hidden_global_offset_z
      - .offset:         384
        .size:           2
        .value_kind:     hidden_grid_dims
      - .offset:         440
        .size:           4
        .value_kind:     hidden_dynamic_lds_size
    .group_segment_fixed_size: 0
    .kernarg_segment_align: 8
    .kernarg_segment_size: 576
    .language:       OpenCL C
    .language_version:
      - 2
      - 0
    .max_flat_workgroup_size: 512
    .name:           _ZN2mk3fwdENS_4ArgsE
    .private_segment_fixed_size: 0
    .sgpr_count:     108
    .sgpr_spill_count: 275
    .symbol:         _ZN2mk3fwdENS_4ArgsE.kd
    .uniform_work_group_size: 1
    .uses_dynamic_stack: false
    .vgpr_count:     256
    .vgpr_spill_count: 0
    .wavefront_size: 64
